# csr pass A: each thread reads its edge segment with two 16-byte loads per 8 elements instead of 8 predicated dword loads
# speedup vs baseline: 1.0159x; 1.0159x over previous
.Lpa_loop:
	global_load_dwordx4 v[26:29], v[10:11], off offset:-16
	global_load_dwordx4 v[30:33], v[10:11], off
	s_add_i32 s12, s3, 1
	v_cmp_lt_i32_e64 s[46:47], s12, v1
	s_add_i32 s12, s3, 2
	v_cmp_lt_i32_e64 s[48:49], s12, v1
	s_add_i32 s12, s3, 3
	v_cmp_lt_i32_e64 s[50:51], s12, v1
	s_add_i32 s12, s3, 4
	v_cmp_lt_i32_e64 s[52:53], s12, v1
	s_add_i32 s12, s3, 5
	v_cmp_lt_i32_e64 s[54:55], s12, v1
	s_add_i32 s12, s3, 6
	v_cmp_lt_i32_e64 s[56:57], s12, v1
	s_add_i32 s12, s3, 7
	v_cmp_lt_i32_e64 s[58:59], s12, v1
	s_mov_b64 s[44:45], exec
	s_and_b64 vcc, exec, s[10:11]
	s_waitcnt vmcnt(0)
	s_cbranch_vccnz .Lpa_generic
	ds_write_b32 v22, v26
	v_lshlrev_b32_sdwa v26, v24, v26 dst_sel:DWORD dst_unused:UNUSED_PAD src0_sel:DWORD src1_sel:WORD_1
	ds_add_u32 v26, v23 offset:24848
	s_mov_b64 exec, s[46:47]
	ds_write_b32 v22, v27 offset:4
	v_lshlrev_b32_sdwa v27, v24, v27 dst_sel:DWORD dst_unused:UNUSED_PAD src0_sel:DWORD src1_sel:WORD_1
	ds_add_u32 v27, v23 offset:24848
	s_mov_b64 exec, s[48:49]
	ds_write_b32 v22, v28 offset:8
	v_lshlrev_b32_sdwa v28, v24, v28 dst_sel:DWORD dst_unused:UNUSED_PAD src0_sel:DWORD src1_sel:WORD_1
	ds_add_u32 v28, v23 offset:24848
	s_mov_b64 exec, s[50:51]
	ds_write_b32 v22, v29 offset:12
	v_lshlrev_b32_sdwa v29, v24, v29 dst_sel:DWORD dst_unused:UNUSED_PAD src0_sel:DWORD src1_sel:WORD_1
	ds_add_u32 v29, v23 offset:24848
	s_mov_b64 exec, s[52:53]
	ds_write_b32 v22, v30 offset:16
	v_lshlrev_b32_sdwa v30, v24, v30 dst_sel:DWORD dst_unused:UNUSED_PAD src0_sel:DWORD src1_sel:WORD_1
	ds_add_u32 v30, v23 offset:24848
	s_mov_b64 exec, s[54:55]
	ds_write_b32 v22, v31 offset:20
	v_lshlrev_b32_sdwa v31, v24, v31 dst_sel:DWORD dst_unused:UNUSED_PAD src0_sel:DWORD src1_sel:WORD_1
	ds_add_u32 v31, v23 offset:24848
	s_mov_b64 exec, s[56:57]
	ds_write_b32 v22, v32 offset:24
	v_lshlrev_b32_sdwa v32, v24, v32 dst_sel:DWORD dst_unused:UNUSED_PAD src0_sel:DWORD src1_sel:WORD_1
	ds_add_u32 v32, v23 offset:24848
	s_mov_b64 exec, s[58:59]
	ds_write_b32 v22, v33 offset:28
	v_lshlrev_b32_sdwa v33, v24, v33 dst_sel:DWORD dst_unused:UNUSED_PAD src0_sel:DWORD src1_sel:WORD_1
	ds_add_u32 v33, v23 offset:24848
	s_branch .Lpa_next
.Lpa_generic:
	v_lshlrev_b32_sdwa v26, v24, v26 dst_sel:DWORD dst_unused:UNUSED_PAD src0_sel:DWORD src1_sel:WORD_1
	ds_add_u32 v26, v23 offset:24848
	s_mov_b64 exec, s[46:47]
	v_lshlrev_b32_sdwa v27, v24, v27 dst_sel:DWORD dst_unused:UNUSED_PAD src0_sel:DWORD src1_sel:WORD_1
	ds_add_u32 v27, v23 offset:24848
	s_mov_b64 exec, s[48:49]
	v_lshlrev_b32_sdwa v28, v24, v28 dst_sel:DWORD dst_unused:UNUSED_PAD src0_sel:DWORD src1_sel:WORD_1
	ds_add_u32 v28, v23 offset:24848
	s_mov_b64 exec, s[50:51]
	v_lshlrev_b32_sdwa v29, v24, v29 dst_sel:DWORD dst_unused:UNUSED_PAD src0_sel:DWORD src1_sel:WORD_1
	ds_add_u32 v29, v23 offset:24848
	s_mov_b64 exec, s[52:53]
	v_lshlrev_b32_sdwa v30, v24, v30 dst_sel:DWORD dst_unused:UNUSED_PAD src0_sel:DWORD src1_sel:WORD_1
	ds_add_u32 v30, v23 offset:24848
	s_mov_b64 exec, s[54:55]
	v_lshlrev_b32_sdwa v31, v24, v31 dst_sel:DWORD dst_unused:UNUSED_PAD src0_sel:DWORD src1_sel:WORD_1
	ds_add_u32 v31, v23 offset:24848
	s_mov_b64 exec, s[56:57]
	v_lshlrev_b32_sdwa v32, v24, v32 dst_sel:DWORD dst_unused:UNUSED_PAD src0_sel:DWORD src1_sel:WORD_1
	ds_add_u32 v32, v23 offset:24848
	s_mov_b64 exec, s[58:59]
	v_lshlrev_b32_sdwa v33, v24, v33 dst_sel:DWORD dst_unused:UNUSED_PAD src0_sel:DWORD src1_sel:WORD_1
	ds_add_u32 v33, v23 offset:24848
.Lpa_next:
	s_mov_b64 exec, s[44:45]
	s_add_i32 s3, s3, 8
	v_cmp_ge_i32_e32 vcc, s3, v1
	v_add_u32_e32 v22, 32, v22
	s_or_b64 s[42:43], vcc, s[42:43]
	v_lshl_add_u64 v[10:11], v[10:11], 0, 32
	s_andn2_b64 exec, exec, s[42:43]
	s_cbranch_execnz .Lpa_loop
